# token lists through a per-wave LDS byte table instead of ballot/ff1/bpermute chains; look-ahead word carries the block-need bits so prefetched waves skip the masks; reference-max read overlapped with
# speedup vs baseline: 1.0217x; 1.0135x over previous
; #define LAS __attribute__((address_space(3)))
; __device__ __forceinline__ float ex2(float x) { return __builtin_amdgcn_exp2f(x); }
; template <int C>
; __device__ __forceinline__ void attn_far1_fast(const LAS unsigned char* kb, const LAS unsigned char* vb, const bf16x8 (&qf)[2][2], int col, int q, float bias_far, bool sel, Softmax (&st)[2], f32x4 (&O)[2][4]) {
;     const f32x4 z4 = (f32x4){0.f, 0.f, 0.f, 0.f};
;     const float NEG = -__builtin_inff();
;     f32x4 S[4];
; #pragma unroll
;     for (int kt = 0; kt < 4; ++kt) { const bf16x8 k0 = lds_frag(kb, 16 * kt + col, q), k1 = lds_frag(kb, 16 * kt + col, 4 + q);
;         S[kt] = __builtin_amdgcn_mfma_f32_16x16x32_bf16(k0, qf[C][0], z4, 0, 0, 0); S[kt] = __builtin_amdgcn_mfma_f32_16x16x32_bf16(k1, qf[C][1], S[kt], 0, 0, 0); }
;     const float off = (sel ? bias_far : NEG) - st[C].m;
; #pragma unroll
;     for (int kt = 0; kt < 4; ++kt) { f32x4 p = S[kt] + off;
; #pragma unroll
;         for (int e = 0; e < 4; ++e) p[e] = ex2(p[e]);
;         S[kt] = p; }
;     const bf16x8 pf0 = pack8(S[0], S[1]), pf1 = pack8(S[2], S[3]);
.Lbm_step:
	s_mov_b32 s98, 1
	s_cmp_eq_u32 s100, s75
	s_cbranch_scc0 .Lbm_slow
	s_and_b32 s83, s1, 0x4000
	s_add_i32 s99, s1, 0x2000
	s_and_b32 s99, s99, 0x6000
	v_mov_b32_e32 v112, s20
	v_mov_b32_e32 v113, s20
	v_mov_b32_e32 v114, s20
	v_mov_b32_e32 v115, s20
	v_lshrrev_b32_e32 v56, 31, v251
	v_xor_b32_e32 v56, 1, v56
	v_max_i32_e32 v55, 0, v251
	v_mov_b32_e32 v79, v56
	v_and_b32_e32 v54, 63, v55
	v_bfe_u32 v58, v55, 6, 1
	v_bfe_u32 v59, v55, 7, 1
	v_lshl_add_u32 v63, v54, 4, v249
	ds_read_b32 v199, v63
	v_mul_u32_u24_e32 v83, 0x410, v54
	v_cmp_ne_u32_e32 vcc, 0, v58
	v_add_u32_e32 v83, v83, v248
	s_nop 0
	v_cndmask_b32_e32 v81, v2, v154, vcc
	s_cmp_lg_u64 vcc, 0
	s_cselect_b32 s21, 1, 0
	v_cmp_ne_u32_e32 vcc, 0, v59
	s_nop 1
	v_cndmask_b32_e32 v82, v2, v154, vcc
	s_cmp_lg_u64 vcc, 0
	s_cselect_b32 s32, 1, 0
	s_waitcnt vmcnt(4)
	s_and_b32 s77, s21, s32
	s_cmp_eq_u32 s77, 1
	s_cbranch_scc1 .Lbm_full_f
	s_mov_b32 s77, s83
	s_cmp_eq_u32 s21, 1
	s_cbranch_scc1 .Lbm_half_f
	s_mov_b32 s77, s99
	v_mov_b32_e32 v81, v82
.Lbm_half_f:
	v_add_u32_e32 v148, s77, v192
	v_add_u32_e32 v149, v148, v195
	v_add_u32_e32 v148, v148, v193
	ds_read_b128 v[116:119], v148
	ds_read_b128 v[120:123], v149
	ds_read_b128 v[124:127], v148 offset:2048
	ds_read_b128 v[128:131], v149 offset:2048
	ds_read_b128 v[132:135], v148 offset:4096
	ds_read_b128 v[136:139], v149 offset:4096
	ds_read_b128 v[140:143], v148 offset:6144
	ds_read_b128 v[144:147], v149 offset:6144
	s_waitcnt lgkmcnt(8)
	v_sub_f32_e32 v81, v81, v199
	v_sub_f32_e32 v82, v82, v199
	v_mov_b32_e32 v54, v81
	v_mov_b32_e32 v55, v81
	v_mov_b32_e32 v56, v81
	v_mov_b32_e32 v57, v81
	s_mov_b32 s83, -1
	s_add_i32 s77, s75, 2
	s_cmp_gt_i32 s77, s26
	s_cbranch_scc1 .Lbm_g1_end_hf
	s_lshr_b32 s21, s77, 5
	v_mov_b32_e32 v255, v242
	s_cmp_eq_u32 s21, 1
	s_cselect_b64 vcc, -1, 0
	v_cndmask_b32_e32 v255, v255, v243, vcc
	s_cmp_eq_u32 s21, 2
	s_cselect_b64 vcc, -1, 0
	v_cndmask_b32_e32 v255, v255, v244, vcc
	s_cmp_eq_u32 s21, 3
	s_cselect_b64 vcc, -1, 0
	v_cndmask_b32_e32 v255, v255, v245, vcc
	s_and_b32 s21, s77, 31
	s_lshl_b32 s21, 1, s21
	s_lshl_b32 s32, s21, 1
	v_and_b32_e32 v80, s21, v255
	v_cmp_ne_u32_e64 s[12:13], 0, v80
	v_and_b32_e32 v80, s32, v255
	v_cmp_ne_u32_e64 s[14:15], 0, v80
	s_nop 3
	s_or_b64 s[22:23], s[12:13], s[14:15]
	s_bcnt1_i32_b64 s11, s[22:23]
	s_add_i32 s11, s11, 3
	s_lshr_b32 s11, s11, 2
	s_cmp_ge_u32 s91, s11
	s_cbranch_scc1 .Lbm_g1_end_hf
	s_add_i32 s83, s91, 8
	s_cmp_lt_u32 s83, s11
	s_cselect_b32 s83, 0x10000, 0
	s_add_i32 s83, s83, s75
	s_add_i32 s83, s83, 2
	s_andn2_b64 s[84:85], s[12:13], s[14:15]
	s_bcnt1_i32_b64 s77, s[84:85]
	v_mbcnt_lo_u32_b32 v80, s84, 0
	v_mbcnt_hi_u32_b32 v80, s85, v80
	v_mov_b32_e32 v255, s77
	s_and_b64 s[84:85], s[12:13], s[14:15]
	s_bcnt1_i32_b64 s32, s[84:85]
	v_mbcnt_lo_u32_b32 v255, s84, v255
	v_mbcnt_hi_u32_b32 v255, s85, v255
	s_add_i32 s77, s77, s32
	v_cndmask_b32_e64 v80, v80, v255, s[84:85]
	v_mov_b32_e32 v255, s77
	s_andn2_b64 s[84:85], s[14:15], s[12:13]
	v_mbcnt_lo_u32_b32 v255, s84, v255
	v_mbcnt_hi_u32_b32 v255, s85, v255
	s_nop 0
	v_cndmask_b32_e64 v80, v80, v255, s[84:85]
	v_cndmask_b32_e64 v78, 0, 1, s[12:13]
	v_cndmask_b32_e64 v255, 0, 2, s[14:15]
	v_or_b32_e32 v78, v78, v255
	v_and_b32_e32 v255, 63, v185
	v_lshl_or_b32 v78, v78, 6, v255
	s_lshl_b32 s77, s91, 6
	s_add_i32 s77, s77, 0x20900
	v_add_u32_e32 v255, s77, v80
	s_and_saveexec_b64 s[84:85], s[22:23]
	ds_write_b8 v255, v78
	s_mov_b64 exec, s[84:85]
	s_lshl_b32 s32, s91, 2
	s_bcnt1_i32_b64 s84, s[22:23]
	v_lshrrev_b32_e32 v78, 2, v250
	v_add_u32_e32 v78, s32, v78
	v_cmp_gt_u32_e32 vcc, s84, v78
	v_add_u32_e32 v255, s77, v78
	ds_read_u8 v251, v255
	v_cndmask_b32_e64 v254, -1, 0, vcc
.Lbm_g1_end_hf:
	s_waitcnt lgkmcnt(6)
	v_mfma_f32_16x16x32_bf16 v[70:73], v[116:119], v[104:107], v[54:57]
	v_mfma_f32_16x16x32_bf16 v[70:73], v[120:123], v[108:111], v[70:73]
	s_waitcnt lgkmcnt(4)
	v_mfma_f32_16x16x32_bf16 v[74:77], v[124:127], v[104:107], v[54:57]
	v_mfma_f32_16x16x32_bf16 v[74:77], v[128:131], v[108:111], v[74:77]
	ds_read_b128 v[116:119], v148 offset:32768
	ds_read_b128 v[120:123], v149 offset:32768
	ds_read_b128 v[124:127], v148 offset:34816
	ds_read_b128 v[128:131], v149 offset:34816
	s_waitcnt lgkmcnt(6)
	v_mfma_f32_16x16x32_bf16 v[200:203], v[132:135], v[104:107], v[54:57]
	v_mfma_f32_16x16x32_bf16 v[200:203], v[136:139], v[108:111], v[200:203]
	s_waitcnt lgkmcnt(4)
	v_mfma_f32_16x16x32_bf16 v[204:207], v[140:143], v[104:107], v[54:57]
	v_mfma_f32_16x16x32_bf16 v[204:207], v[144:147], v[108:111], v[204:207]
	ds_read_b128 v[132:135], v148 offset:36864
	ds_read_b128 v[136:139], v149 offset:36864
	ds_read_b128 v[140:143], v148 offset:38912
	ds_read_b128 v[144:147], v149 offset:38912
	s_mov_b32 s100, -1
	s_cmp_lt_i32 s83, 0
	s_cbranch_scc1 .Lbm_g2_end_hf
	s_waitcnt lgkmcnt(8)
	v_or_b32_e32 v251, v251, v254
	v_max_i32_e32 v254, 0, v251
	v_and_b32_e32 v254, 63, v254
	v_lshlrev_b32_e32 v254, 11, v254
	v_mov_b32_e32 v255, 0
	v_lshl_add_u64 v[254:255], v[254:255], 0, v[246:247]
	global_load_dwordx4 v[104:107], v[254:255], off
	global_load_dwordx4 v[108:111], v[254:255], off offset:64
	s_mov_b32 s100, s83

; #define LAS __attribute__((address_space(3)))
; template <bool SELMASK>
; __device__ __forceinline__ void attn_far_fast(const LAS unsigned char* kb, const LAS unsigned char* vb, const bf16x8 (&qf)[2][2], int col, int q, float bias_far, bool sel0, bool sel1, Softmax (&st)[2], f32x4 (&O)[2][4]) {
;     const f32x4 z4 = (f32x4){0.f, 0.f, 0.f, 0.f};
;     const float NEG = -__builtin_inff();
;     f32x4 S[2][4];
; #pragma unroll
;     for (int kt = 0; kt < 4; ++kt) { const bf16x8 k0 = lds_frag(kb, 16 * kt + col, q), k1 = lds_frag(kb, 16 * kt + col, 4 + q);
; #pragma unroll
;         for (int c = 0; c < 2; ++c) { S[c][kt] = __builtin_amdgcn_mfma_f32_16x16x32_bf16(k0, qf[c][0], z4, 0, 0, 0); S[c][kt] = __builtin_amdgcn_mfma_f32_16x16x32_bf16(k1, qf[c][1], S[c][kt], 0, 0, 0); } }
;     bf16x8 pf[2][2];
; #pragma unroll
;     for (int c = 0; c < 2; ++c) {
;         const bool sel = c == 0 ? sel0 : sel1;
;         const float off = ((SELMASK && !sel) ? NEG : bias_far) - st[c].m;
.Lbm_full_f:
	v_add_u32_e32 v148, s83, v192
	v_add_u32_e32 v149, v148, v195
	v_add_u32_e32 v148, v148, v193
	ds_read_b128 v[116:119], v148
	ds_read_b128 v[120:123], v149
	ds_read_b128 v[124:127], v148 offset:2048
	ds_read_b128 v[128:131], v149 offset:2048
	ds_read_b128 v[132:135], v148 offset:4096
	ds_read_b128 v[136:139], v149 offset:4096
	ds_read_b128 v[140:143], v148 offset:6144
	ds_read_b128 v[144:147], v149 offset:6144
	v_add_u32_e32 v208, s99, v192
	v_add_u32_e32 v209, v208, v195
	v_add_u32_e32 v208, v208, v193
	ds_read_b128 v[38:41], v208
	ds_read_b128 v[42:45], v209
	ds_read_b128 v[46:49], v208 offset:2048
	ds_read_b128 v[50:53], v209 offset:2048
	s_waitcnt lgkmcnt(12)
	v_sub_f32_e32 v81, v81, v199
	v_sub_f32_e32 v82, v82, v199
	v_mov_b32_e32 v70, v81
	v_mov_b32_e32 v71, v81
	v_mov_b32_e32 v72, v81
	v_mov_b32_e32 v73, v81
	v_mov_b32_e32 v74, v81
	v_mov_b32_e32 v75, v81
	v_mov_b32_e32 v76, v81
	v_mov_b32_e32 v77, v81
	v_mov_b32_e32 v200, v81
	v_mov_b32_e32 v201, v81
	v_mov_b32_e32 v202, v81
	v_mov_b32_e32 v203, v81
	v_mov_b32_e32 v204, v81
	v_mov_b32_e32 v205, v81
	v_mov_b32_e32 v206, v81
	v_mov_b32_e32 v207, v81
	v_mov_b32_e32 v54, v82
	v_mov_b32_e32 v55, v82
	v_mov_b32_e32 v56, v82
	v_mov_b32_e32 v57, v82
	v_mov_b32_e32 v58, v82
	v_mov_b32_e32 v59, v82
	v_mov_b32_e32 v60, v82
	v_mov_b32_e32 v61, v82
	v_mov_b32_e32 v62, v82
	v_mov_b32_e32 v63, v82
	v_mov_b32_e32 v64, v82
	v_mov_b32_e32 v65, v82
	v_mov_b32_e32 v66, v82
	v_mov_b32_e32 v67, v82
	v_mov_b32_e32 v68, v82
	v_mov_b32_e32 v69, v82
	s_mov_b32 s83, -1
	s_add_i32 s77, s75, 2
	s_cmp_gt_i32 s77, s26
	s_cbranch_scc1 .Lbm_g1_end_af
	s_lshr_b32 s21, s77, 5
	v_mov_b32_e32 v255, v242
	s_cmp_eq_u32 s21, 1
	s_cselect_b64 vcc, -1, 0
	v_cndmask_b32_e32 v255, v255, v243, vcc
	s_cmp_eq_u32 s21, 2
	s_cselect_b64 vcc, -1, 0
	v_cndmask_b32_e32 v255, v255, v244, vcc
	s_cmp_eq_u32 s21, 3
	s_cselect_b64 vcc, -1, 0
	v_cndmask_b32_e32 v255, v255, v245, vcc
	s_and_b32 s21, s77, 31
	s_lshl_b32 s21, 1, s21
	s_lshl_b32 s32, s21, 1
	v_and_b32_e32 v80, s21, v255
	v_cmp_ne_u32_e64 s[12:13], 0, v80
	v_and_b32_e32 v80, s32, v255
	v_cmp_ne_u32_e64 s[14:15], 0, v80
	s_nop 3
	s_or_b64 s[22:23], s[12:13], s[14:15]
	s_bcnt1_i32_b64 s11, s[22:23]
	s_add_i32 s11, s11, 3
	s_lshr_b32 s11, s11, 2
	s_cmp_ge_u32 s91, s11
	s_cbranch_scc1 .Lbm_g1_end_af
	s_add_i32 s83, s91, 8
	s_cmp_lt_u32 s83, s11
	s_cselect_b32 s83, 0x10000, 0
	s_add_i32 s83, s83, s75
	s_add_i32 s83, s83, 2
	s_andn2_b64 s[84:85], s[12:13], s[14:15]
	s_bcnt1_i32_b64 s77, s[84:85]
	v_mbcnt_lo_u32_b32 v80, s84, 0
	v_mbcnt_hi_u32_b32 v80, s85, v80
	v_mov_b32_e32 v255, s77
	s_and_b64 s[84:85], s[12:13], s[14:15]
	s_bcnt1_i32_b64 s32, s[84:85]
	v_mbcnt_lo_u32_b32 v255, s84, v255
	v_mbcnt_hi_u32_b32 v255, s85, v255
	s_add_i32 s77, s77, s32
	v_cndmask_b32_e64 v80, v80, v255, s[84:85]
	v_mov_b32_e32 v255, s77
	s_andn2_b64 s[84:85], s[14:15], s[12:13]
	v_mbcnt_lo_u32_b32 v255, s84, v255
	v_mbcnt_hi_u32_b32 v255, s85, v255
	s_nop 0
	v_cndmask_b32_e64 v80, v80, v255, s[84:85]
	v_cndmask_b32_e64 v78, 0, 1, s[12:13]
	v_cndmask_b32_e64 v255, 0, 2, s[14:15]
	v_or_b32_e32 v78, v78, v255
	v_and_b32_e32 v255, 63, v185
	v_lshl_or_b32 v78, v78, 6, v255
	s_lshl_b32 s77, s91, 6
	s_add_i32 s77, s77, 0x20900
	v_add_u32_e32 v255, s77, v80
	s_and_saveexec_b64 s[84:85], s[22:23]
	ds_write_b8 v255, v78
	s_mov_b64 exec, s[84:85]
	s_lshl_b32 s32, s91, 2
	s_bcnt1_i32_b64 s84, s[22:23]
	v_lshrrev_b32_e32 v78, 2, v250
	v_add_u32_e32 v78, s32, v78
	v_cmp_gt_u32_e32 vcc, s84, v78
	v_add_u32_e32 v255, s77, v78
	ds_read_u8 v251, v255
	v_cndmask_b32_e64 v254, -1, 0, vcc
; __device__ __forceinline__ float ex2(float x) { return __builtin_amdgcn_exp2f(x); }
; template <bool SELMASK>
; __device__ __forceinline__ void attn_far_fast(const LAS unsigned char* kb, const LAS unsigned char* vb, const bf16x8 (&qf)[2][2], int col, int q, float bias_far, bool sel0, bool sel1, Softmax (&st)[2], f32x4 (&O)[2][4]) {
;     ...
; #pragma unroll
;     for (int kt = 0; kt < 4; ++kt) { const bf16x8 k0 = lds_frag(kb, 16 * kt + col, q), k1 = lds_frag(kb, 16 * kt + col, 4 + q);
; #pragma unroll
;         for (int c = 0; c < 2; ++c) { S[c][kt] = __builtin_amdgcn_mfma_f32_16x16x32_bf16(k0, qf[c][0], z4, 0, 0, 0); S[c][kt] = __builtin_amdgcn_mfma_f32_16x16x32_bf16(k1, qf[c][1], S[c][kt], 0, 0, 0); } }
;     bf16x8 pf[2][2];
; #pragma unroll
;     for (int c = 0; c < 2; ++c) {
;         const bool sel = c == 0 ? sel0 : sel1;
;         const float off = ((SELMASK && !sel) ? NEG : bias_far) - st[c].m;
; #pragma unroll
;         for (int kt = 0; kt < 4; ++kt) { f32x4 p = S[c][kt] + off;
; #pragma unroll
;             for (int e = 0; e < 4; ++e) p[e] = ex2(p[e]);
;             S[c][kt] = p; }
;         pf[c][0] = pack8(S[c][0], S[c][1]); pf[c][1] = pack8(S[c][2], S[c][3]);
;         st[c].l = __builtin_amdgcn_mfma_f32_16x16x32_bf16(ONES8, pf[c][0], st[c].l, 0, 0, 0); st[c].l = __builtin_amdgcn_mfma_f32_16x16x32_bf16(ONES8, pf[c][1], st[c].l, 0, 0, 0);
;     }
; #pragma unroll
;     for (int c32 = 0; c32 < 2; ++c32)
; #pragma unroll
;         for (int dt = 0; dt < 4; ++dt) { const bf16x8 vf = lds_frag(vb, 16 * dt + col, 4 * c32 + q);
;             O[0][dt] = __builtin_amdgcn_mfma_f32_16x16x32_bf16(vf, pf[0][c32], O[0][dt], 0, 0, 0);
;             O[1][dt] = __builtin_amdgcn_mfma_f32_16x16x32_bf16(vf, pf[1][c32], O[1][dt], 0, 0, 0); }
.Lbm_g1_end_af:
	s_waitcnt lgkmcnt(10)
	v_mfma_f32_16x16x32_bf16 v[70:73], v[116:119], v[104:107], v[70:73]
	v_mfma_f32_16x16x32_bf16 v[70:73], v[120:123], v[108:111], v[70:73]
	s_waitcnt lgkmcnt(8)
	v_mfma_f32_16x16x32_bf16 v[74:77], v[124:127], v[104:107], v[74:77]
	v_mfma_f32_16x16x32_bf16 v[74:77], v[128:131], v[108:111], v[74:77]
	ds_read_b128 v[116:119], v148 offset:32768
	ds_read_b128 v[120:123], v149 offset:32768
	ds_read_b128 v[124:127], v148 offset:34816
	ds_read_b128 v[128:131], v149 offset:34816
	s_waitcnt lgkmcnt(10)
	v_mfma_f32_16x16x32_bf16 v[200:203], v[132:135], v[104:107], v[200:203]
	v_mfma_f32_16x16x32_bf16 v[200:203], v[136:139], v[108:111], v[200:203]
	s_waitcnt lgkmcnt(8)
	v_mfma_f32_16x16x32_bf16 v[204:207], v[140:143], v[104:107], v[204:207]
	v_mfma_f32_16x16x32_bf16 v[204:207], v[144:147], v[108:111], v[204:207]
	ds_read_b128 v[132:135], v148 offset:36864
	ds_read_b128 v[136:139], v149 offset:36864
	ds_read_b128 v[140:143], v148 offset:38912
	ds_read_b128 v[144:147], v149 offset:38912
	s_waitcnt lgkmcnt(10)
	v_mfma_f32_16x16x32_bf16 v[54:57], v[38:41], v[104:107], v[54:57]
	v_mfma_f32_16x16x32_bf16 v[54:57], v[42:45], v[108:111], v[54:57]
	s_waitcnt lgkmcnt(8)
	v_mfma_f32_16x16x32_bf16 v[58:61], v[46:49], v[104:107], v[58:61]
	v_mfma_f32_16x16x32_bf16 v[58:61], v[50:53], v[108:111], v[58:61]
	ds_read_b128 v[38:41], v208 offset:4096
	ds_read_b128 v[42:45], v209 offset:4096
	ds_read_b128 v[46:49], v208 offset:6144
	ds_read_b128 v[50:53], v209 offset:6144
	v_exp_f32_e32 v70, v70
	v_exp_f32_e32 v71, v71
	v_exp_f32_e32 v72, v72
	v_exp_f32_e32 v73, v73
	v_exp_f32_e32 v74, v74
	v_exp_f32_e32 v75, v75
	v_exp_f32_e32 v76, v76
	v_exp_f32_e32 v77, v77
	v_exp_f32_e32 v200, v200
	v_exp_f32_e32 v201, v201
	v_exp_f32_e32 v202, v202
	v_exp_f32_e32 v203, v203
	v_exp_f32_e32 v204, v204
	v_exp_f32_e32 v205, v205
	v_exp_f32_e32 v206, v206
	v_exp_f32_e32 v207, v207
	s_nop 0
	v_cvt_pk_bf16_f32 v70, v70, v71
	v_cvt_pk_bf16_f32 v71, v72, v73
	v_cvt_pk_bf16_f32 v72, v74, v75
	v_cvt_pk_bf16_f32 v73, v76, v77
	v_cvt_pk_bf16_f32 v74, v200, v201
	v_cvt_pk_bf16_f32 v75, v202, v203
	v_cvt_pk_bf16_f32 v76, v204, v205
	v_cvt_pk_bf16_f32 v77, v206, v207
	s_nop 1
	v_mfma_f32_16x16x32_bf16 v[100:103], v[112:115], v[70:73], 0
	v_mfma_f32_16x16x32_bf16 v[100:103], v[112:115], v[74:77], v[100:103]
	s_waitcnt lgkmcnt(4)
	v_mfma_f32_16x16x32_bf16 v[84:87], v[116:119], v[70:73], 0
	v_mfma_f32_16x16x32_bf16 v[84:87], v[120:123], v[74:77], v[84:87]
	v_mfma_f32_16x16x32_bf16 v[88:91], v[124:127], v[70:73], 0
	v_mfma_f32_16x16x32_bf16 v[88:91], v[128:131], v[74:77], v[88:91]
	v_mfma_f32_16x16x32_bf16 v[92:95], v[132:135], v[70:73], 0
	v_mfma_f32_16x16x32_bf16 v[92:95], v[136:139], v[74:77], v[92:95]
	v_mfma_f32_16x16x32_bf16 v[96:99], v[140:143], v[70:73], 0
	v_mfma_f32_16x16x32_bf16 v[96:99], v[144:147], v[74:77], v[96:99]
	s_waitcnt lgkmcnt(2)
	v_mfma_f32_16x16x32_bf16 v[62:65], v[38:41], v[104:107], v[62:65]
	v_mfma_f32_16x16x32_bf16 v[62:65], v[42:45], v[108:111], v[62:65]
	s_waitcnt lgkmcnt(0)
	v_mfma_f32_16x16x32_bf16 v[66:69], v[46:49], v[104:107], v[66:69]
	v_mfma_f32_16x16x32_bf16 v[66:69], v[50:53], v[108:111], v[66:69]
	ds_read_b128 v[116:119], v208 offset:32768
	ds_read_b128 v[120:123], v209 offset:32768
	ds_read_b128 v[124:127], v208 offset:34816
	ds_read_b128 v[128:131], v209 offset:34816
	ds_read_b128 v[132:135], v208 offset:36864
	ds_read_b128 v[136:139], v209 offset:36864
	ds_read_b128 v[140:143], v208 offset:38912
	ds_read_b128 v[144:147], v209 offset:38912
	s_mov_b32 s100, -1
	s_cmp_lt_i32 s83, 0
	s_cbranch_scc1 .Lbm_g2_end_af
	s_waitcnt lgkmcnt(8)
	v_or_b32_e32 v251, v251, v254
	v_max_i32_e32 v254, 0, v251
	v_and_b32_e32 v254, 63, v254
	v_lshlrev_b32_e32 v254, 11, v254
	v_mov_b32_e32 v255, 0
	v_lshl_add_u64 v[254:255], v[254:255], 0, v[246:247]
	global_load_dwordx4 v[104:107], v[254:255], off
	global_load_dwordx4 v[108:111], v[254:255], off offset:64
	s_mov_b32 s100, s83

.Lbm_slow:
	s_lshr_b32 s21, s75, 5
	v_mov_b32_e32 v79, v242
	s_cmp_eq_u32 s21, 1
	s_cselect_b64 vcc, -1, 0
	v_cndmask_b32_e32 v79, v79, v243, vcc
	s_cmp_eq_u32 s21, 2
	s_cselect_b64 vcc, -1, 0
	v_cndmask_b32_e32 v79, v79, v244, vcc
	s_cmp_eq_u32 s21, 3
	s_cselect_b64 vcc, -1, 0
	v_cndmask_b32_e32 v79, v79, v245, vcc
	s_and_b32 s21, s75, 31
	s_lshl_b32 s21, 1, s21
	s_lshl_b32 s32, s21, 1
	v_and_b32_e32 v80, s21, v79
	v_cmp_ne_u32_e64 s[12:13], 0, v80
	v_and_b32_e32 v80, s32, v79
	v_cmp_ne_u32_e64 s[14:15], 0, v80
	s_nop 3
	s_or_b64 s[22:23], s[12:13], s[14:15]
	s_bcnt1_i32_b64 s11, s[22:23]
	s_add_i32 s11, s11, 3
	s_lshr_b32 s11, s11, 2
	s_cmp_ge_u32 s91, s11
	s_cbranch_scc1 .Lbm_noitem
	s_and_b32 s83, s1, 0x4000
	s_add_i32 s99, s1, 0x2000
	s_and_b32 s99, s99, 0x6000
	v_mov_b32_e32 v112, s20
	v_mov_b32_e32 v113, s20
	v_mov_b32_e32 v114, s20
	v_mov_b32_e32 v115, s20
	s_add_i32 s101, s91, 8
	s_cmp_lt_u32 s101, s11
	s_cselect_b32 s101, 1, 0
	s_and_b32 s77, s100, 0xffff
	s_cmp_eq_u32 s77, s75
	s_cbranch_scc1 .Lbm_r1_pf
	s_andn2_b64 s[84:85], s[12:13], s[14:15]
	s_bcnt1_i32_b64 s77, s[84:85]
	v_mbcnt_lo_u32_b32 v80, s84, 0
	v_mbcnt_hi_u32_b32 v80, s85, v80
	v_mov_b32_e32 v56, s77
	s_and_b64 s[84:85], s[12:13], s[14:15]
	s_bcnt1_i32_b64 s32, s[84:85]
	v_mbcnt_lo_u32_b32 v56, s84, v56
	v_mbcnt_hi_u32_b32 v56, s85, v56
	s_add_i32 s77, s77, s32
	v_cndmask_b32_e64 v80, v80, v56, s[84:85]
	v_mov_b32_e32 v56, s77
	s_andn2_b64 s[84:85], s[14:15], s[12:13]
	v_mbcnt_lo_u32_b32 v56, s84, v56
	v_mbcnt_hi_u32_b32 v56, s85, v56
	s_nop 0
	v_cndmask_b32_e64 v80, v80, v56, s[84:85]
	v_cndmask_b32_e64 v58, 0, 1, s[12:13]
	v_cndmask_b32_e64 v59, 0, 2, s[14:15]
	v_or_b32_e32 v58, v58, v59
	v_and_b32_e32 v59, 63, v185
	v_lshl_or_b32 v58, v58, 6, v59
	s_lshl_b32 s77, s91, 6
	s_add_i32 s77, s77, 0x20900
	v_add_u32_e32 v59, s77, v80
	s_and_saveexec_b64 s[84:85], s[22:23]
	ds_write_b8 v59, v58
	s_mov_b64 exec, s[84:85]
	s_lshl_b32 s32, s91, 2
	s_bcnt1_i32_b64 s84, s[22:23]
	v_lshrrev_b32_e32 v58, 2, v250
	v_add_u32_e32 v58, s32, v58
	v_cmp_gt_u32_e32 vcc, s84, v58
	v_add_u32_e32 v59, s77, v58
	ds_read_u8 v63, v59
	v_cndmask_b32_e64 v60, -1, 0, vcc
	s_waitcnt lgkmcnt(0)
	v_or_b32_e32 v63, v63, v60
	v_lshrrev_b32_e32 v56, 31, v63
	v_xor_b32_e32 v56, 1, v56
	v_max_i32_e32 v55, 0, v63
	v_mov_b32_e32 v79, v56
	v_and_b32_e32 v54, 63, v55
	v_bfe_u32 v58, v55, 6, 1
	v_bfe_u32 v59, v55, 7, 1
	v_lshlrev_b32_e32 v60, 11, v54
	v_mov_b32_e32 v61, 0
	v_lshl_add_u64 v[60:61], v[60:61], 0, v[246:247]
	global_load_dwordx4 v[104:107], v[60:61], off
	global_load_dwordx4 v[108:111], v[60:61], off offset:64
	v_lshl_add_u32 v63, v54, 4, v249
	ds_read_b32 v199, v63
	v_mul_u32_u24_e32 v83, 0x410, v54
	v_cmp_ne_u32_e32 vcc, 0, v58
	v_add_u32_e32 v83, v83, v248
	s_nop 0
	v_cndmask_b32_e32 v81, v2, v154, vcc
	s_cmp_lg_u64 vcc, 0
	s_cselect_b32 s21, 1, 0
	v_cmp_ne_u32_e32 vcc, 0, v59
	s_nop 1
	v_cndmask_b32_e32 v82, v2, v154, vcc
	s_cmp_lg_u64 vcc, 0
	s_cselect_b32 s32, 1, 0
	s_waitcnt vmcnt(0)
	s_branch .Lbm_r1_go
.Lbm_r1_pf:
	v_lshrrev_b32_e32 v56, 31, v251
	v_xor_b32_e32 v56, 1, v56
	v_max_i32_e32 v55, 0, v251
	v_mov_b32_e32 v79, v56
	v_and_b32_e32 v54, 63, v55
	v_bfe_u32 v58, v55, 6, 1
	v_bfe_u32 v59, v55, 7, 1
	v_lshl_add_u32 v63, v54, 4, v249
	ds_read_b32 v199, v63
	v_mul_u32_u24_e32 v83, 0x410, v54
	v_cmp_ne_u32_e32 vcc, 0, v58
	v_add_u32_e32 v83, v83, v248
	s_nop 0
	v_cndmask_b32_e32 v81, v2, v154, vcc
	s_cmp_lg_u64 vcc, 0
	s_cselect_b32 s21, 1, 0
	v_cmp_ne_u32_e32 vcc, 0, v59
	s_nop 1
	v_cndmask_b32_e32 v82, v2, v154, vcc
	s_cmp_lg_u64 vcc, 0
	s_cselect_b32 s32, 1, 0
	s_waitcnt vmcnt(4)

; __device__ __forceinline__ float ex2(float x) { return __builtin_amdgcn_exp2f(x); }
; template <bool SELMASK>
; __device__ __forceinline__ void attn_far_fast(const LAS unsigned char* kb, const LAS unsigned char* vb, const bf16x8 (&qf)[2][2], int col, int q, float bias_far, bool sel0, bool sel1, Softmax (&st)[2], f32x4 (&O)[2][4]) {
;     ...
; #pragma unroll
;     for (int kt = 0; kt < 4; ++kt) { const bf16x8 k0 = lds_frag(kb, 16 * kt + col, q), k1 = lds_frag(kb, 16 * kt + col, 4 + q);
; #pragma unroll
;         for (int c = 0; c < 2; ++c) { S[c][kt] = __builtin_amdgcn_mfma_f32_16x16x32_bf16(k0, qf[c][0], z4, 0, 0, 0); S[c][kt] = __builtin_amdgcn_mfma_f32_16x16x32_bf16(k1, qf[c][1], S[c][kt], 0, 0, 0); } }
;     bf16x8 pf[2][2];
; #pragma unroll
;     for (int c = 0; c < 2; ++c) {
;         const bool sel = c == 0 ? sel0 : sel1;
;         const float off = ((SELMASK && !sel) ? NEG : bias_far) - st[c].m;
; #pragma unroll
;         for (int kt = 0; kt < 4; ++kt) { f32x4 p = S[c][kt] + off;
; #pragma unroll
;             for (int e = 0; e < 4; ++e) p[e] = ex2(p[e]);
;             S[c][kt] = p; }
;         pf[c][0] = pack8(S[c][0], S[c][1]); pf[c][1] = pack8(S[c][2], S[c][3]);
;         st[c].l = __builtin_amdgcn_mfma_f32_16x16x32_bf16(ONES8, pf[c][0], st[c].l, 0, 0, 0); st[c].l = __builtin_amdgcn_mfma_f32_16x16x32_bf16(ONES8, pf[c][1], st[c].l, 0, 0, 0);
;     }
; #pragma unroll
;     for (int c32 = 0; c32 < 2; ++c32)
; #pragma unroll
;         for (int dt = 0; dt < 4; ++dt) { const bf16x8 vf = lds_frag(vb, 16 * dt + col, 4 * c32 + q);
;             O[0][dt] = __builtin_amdgcn_mfma_f32_16x16x32_bf16(vf, pf[0][c32], O[0][dt], 0, 0, 0);
;             O[1][dt] = __builtin_amdgcn_mfma_f32_16x16x32_bf16(vf, pf[1][c32], O[1][dt], 0, 0, 0); }
.Lbm_r1_two:
	v_add_u32_e32 v148, s83, v192
	v_add_u32_e32 v149, v148, v195
	v_add_u32_e32 v148, v148, v193
	ds_read_b128 v[116:119], v148
	ds_read_b128 v[120:123], v149
	ds_read_b128 v[124:127], v148 offset:2048
	ds_read_b128 v[128:131], v149 offset:2048
	ds_read_b128 v[132:135], v148 offset:4096
	ds_read_b128 v[136:139], v149 offset:4096
	ds_read_b128 v[140:143], v148 offset:6144
	ds_read_b128 v[144:147], v149 offset:6144
	v_add_u32_e32 v208, s99, v192
	v_add_u32_e32 v209, v208, v195
	v_add_u32_e32 v208, v208, v193
	ds_read_b128 v[38:41], v208
	ds_read_b128 v[42:45], v209
	ds_read_b128 v[46:49], v208 offset:2048
	ds_read_b128 v[50:53], v209 offset:2048
	s_waitcnt lgkmcnt(12)
	v_sub_f32_e32 v81, v81, v199
	v_sub_f32_e32 v82, v82, v199
	v_mov_b32_e32 v70, v81
	v_mov_b32_e32 v71, v81
	v_mov_b32_e32 v72, v81
	v_mov_b32_e32 v73, v81
	v_mov_b32_e32 v74, v81
	v_mov_b32_e32 v75, v81
	v_mov_b32_e32 v76, v81
	v_mov_b32_e32 v77, v81
	v_mov_b32_e32 v200, v81
	v_mov_b32_e32 v201, v81
	v_mov_b32_e32 v202, v81
	v_mov_b32_e32 v203, v81
	v_mov_b32_e32 v204, v81
	v_mov_b32_e32 v205, v81
	v_mov_b32_e32 v206, v81
	v_mov_b32_e32 v207, v81
	v_mov_b32_e32 v54, v82
	v_mov_b32_e32 v55, v82
	v_mov_b32_e32 v56, v82
	v_mov_b32_e32 v57, v82
	v_mov_b32_e32 v58, v82
	v_mov_b32_e32 v59, v82
	v_mov_b32_e32 v60, v82
	v_mov_b32_e32 v61, v82
	v_mov_b32_e32 v62, v82
	v_mov_b32_e32 v63, v82
	v_mov_b32_e32 v64, v82
	v_mov_b32_e32 v65, v82
	v_mov_b32_e32 v66, v82
	v_mov_b32_e32 v67, v82
	v_mov_b32_e32 v68, v82
	v_mov_b32_e32 v69, v82
	s_waitcnt lgkmcnt(10)
	v_mfma_f32_16x16x32_bf16 v[70:73], v[116:119], v[104:107], v[70:73]
	v_mfma_f32_16x16x32_bf16 v[70:73], v[120:123], v[108:111], v[70:73]
	s_waitcnt lgkmcnt(8)
	v_mfma_f32_16x16x32_bf16 v[74:77], v[124:127], v[104:107], v[74:77]
	v_mfma_f32_16x16x32_bf16 v[74:77], v[128:131], v[108:111], v[74:77]
	ds_read_b128 v[116:119], v148 offset:32768
	ds_read_b128 v[120:123], v149 offset:32768
	ds_read_b128 v[124:127], v148 offset:34816
	ds_read_b128 v[128:131], v149 offset:34816
	s_waitcnt lgkmcnt(10)
	v_mfma_f32_16x16x32_bf16 v[200:203], v[132:135], v[104:107], v[200:203]
	v_mfma_f32_16x16x32_bf16 v[200:203], v[136:139], v[108:111], v[200:203]
	s_waitcnt lgkmcnt(8)
	v_mfma_f32_16x16x32_bf16 v[204:207], v[140:143], v[104:107], v[204:207]
	v_mfma_f32_16x16x32_bf16 v[204:207], v[144:147], v[108:111], v[204:207]
	ds_read_b128 v[132:135], v148 offset:36864
	ds_read_b128 v[136:139], v149 offset:36864
	ds_read_b128 v[140:143], v148 offset:38912
	ds_read_b128 v[144:147], v149 offset:38912
	s_waitcnt lgkmcnt(10)
	v_mfma_f32_16x16x32_bf16 v[54:57], v[38:41], v[104:107], v[54:57]
	v_mfma_f32_16x16x32_bf16 v[54:57], v[42:45], v[108:111], v[54:57]
	s_waitcnt lgkmcnt(8)
	v_mfma_f32_16x16x32_bf16 v[58:61], v[46:49], v[104:107], v[58:61]
	v_mfma_f32_16x16x32_bf16 v[58:61], v[50:53], v[108:111], v[58:61]
	ds_read_b128 v[38:41], v208 offset:4096
	ds_read_b128 v[42:45], v209 offset:4096
	ds_read_b128 v[46:49], v208 offset:6144
	ds_read_b128 v[50:53], v209 offset:6144
	v_exp_f32_e32 v70, v70
	v_exp_f32_e32 v71, v71
	v_exp_f32_e32 v72, v72
	v_exp_f32_e32 v73, v73
	v_exp_f32_e32 v74, v74
	v_exp_f32_e32 v75, v75
	v_exp_f32_e32 v76, v76
	v_exp_f32_e32 v77, v77
	v_exp_f32_e32 v200, v200
	v_exp_f32_e32 v201, v201
	v_exp_f32_e32 v202, v202
	v_exp_f32_e32 v203, v203
	v_exp_f32_e32 v204, v204
	v_exp_f32_e32 v205, v205
	v_exp_f32_e32 v206, v206
	v_exp_f32_e32 v207, v207
	s_nop 0
	v_cvt_pk_bf16_f32 v70, v70, v71
	v_cvt_pk_bf16_f32 v71, v72, v73
	v_cvt_pk_bf16_f32 v72, v74, v75
	v_cvt_pk_bf16_f32 v73, v76, v77
	v_cvt_pk_bf16_f32 v74, v200, v201
	v_cvt_pk_bf16_f32 v75, v202, v203
	v_cvt_pk_bf16_f32 v76, v204, v205
	v_cvt_pk_bf16_f32 v77, v206, v207
	s_nop 1
	v_mfma_f32_16x16x32_bf16 v[100:103], v[112:115], v[70:73], 0
	v_mfma_f32_16x16x32_bf16 v[100:103], v[112:115], v[74:77], v[100:103]
	s_waitcnt lgkmcnt(4)
	v_mfma_f32_16x16x32_bf16 v[84:87], v[116:119], v[70:73], 0
	v_mfma_f32_16x16x32_bf16 v[84:87], v[120:123], v[74:77], v[84:87]
	v_mfma_f32_16x16x32_bf16 v[88:91], v[124:127], v[70:73], 0
	v_mfma_f32_16x16x32_bf16 v[88:91], v[128:131], v[74:77], v[88:91]
	v_mfma_f32_16x16x32_bf16 v[92:95], v[132:135], v[70:73], 0
	v_mfma_f32_16x16x32_bf16 v[92:95], v[136:139], v[74:77], v[92:95]
	v_mfma_f32_16x16x32_bf16 v[96:99], v[140:143], v[70:73], 0
	v_mfma_f32_16x16x32_bf16 v[96:99], v[144:147], v[74:77], v[96:99]
	s_waitcnt lgkmcnt(2)
	v_mfma_f32_16x16x32_bf16 v[62:65], v[38:41], v[104:107], v[62:65]
	v_mfma_f32_16x16x32_bf16 v[62:65], v[42:45], v[108:111], v[62:65]
	s_waitcnt lgkmcnt(0)
	v_mfma_f32_16x16x32_bf16 v[66:69], v[46:49], v[104:107], v[66:69]
	v_mfma_f32_16x16x32_bf16 v[66:69], v[50:53], v[108:111], v[66:69]
	ds_read_b128 v[116:119], v208 offset:32768
	ds_read_b128 v[120:123], v209 offset:32768
	ds_read_b128 v[124:127], v208 offset:34816
	ds_read_b128 v[128:131], v209 offset:34816
	ds_read_b128 v[132:135], v208 offset:36864
	ds_read_b128 v[136:139], v209 offset:36864
	ds_read_b128 v[140:143], v208 offset:38912
	ds_read_b128 v[144:147], v209 offset:38912
	s_nop 3
	v_exp_f32_e32 v54, v54
	v_exp_f32_e32 v55, v55
	v_exp_f32_e32 v56, v56
	v_exp_f32_e32 v57, v57
	v_exp_f32_e32 v58, v58
	v_exp_f32_e32 v59, v59
	v_exp_f32_e32 v60, v60
	v_exp_f32_e32 v61, v61
	v_exp_f32_e32 v62, v62
	v_exp_f32_e32 v63, v63
	v_exp_f32_e32 v64, v64
	v_exp_f32_e32 v65, v65
	v_exp_f32_e32 v66, v66
	v_exp_f32_e32 v67, v67
	v_exp_f32_e32 v68, v68
	v_exp_f32_e32 v69, v69
	s_nop 0
	v_cvt_pk_bf16_f32 v54, v54, v55
	v_cvt_pk_bf16_f32 v55, v56, v57
	v_cvt_pk_bf16_f32 v56, v58, v59
	v_cvt_pk_bf16_f32 v57, v60, v61
	v_cvt_pk_bf16_f32 v58, v62, v63
	v_cvt_pk_bf16_f32 v59, v64, v65
	v_cvt_pk_bf16_f32 v60, v66, v67
	v_cvt_pk_bf16_f32 v61, v68, v69
	s_nop 1
	v_mfma_f32_16x16x32_bf16 v[100:103], v[112:115], v[54:57], v[100:103]
	v_mfma_f32_16x16x32_bf16 v[100:103], v[112:115], v[58:61], v[100:103]
	s_waitcnt lgkmcnt(4)
; template <bool SELMASK>
; __device__ __forceinline__ void attn_far_fast(const LAS unsigned char* kb, const LAS unsigned char* vb, const bf16x8 (&qf)[2][2], int col, int q, float bias_far, bool sel0, bool sel1, Softmax (&st)[2], f32x4 (&O)[2][4]) {
;     ...
; #pragma unroll
;     for (int c32 = 0; c32 < 2; ++c32)
; #pragma unroll
;         for (int dt = 0; dt < 4; ++dt) { const bf16x8 vf = lds_frag(vb, 16 * dt + col, 4 * c32 + q);
;             O[0][dt] = __builtin_amdgcn_mfma_f32_16x16x32_bf16(vf, pf[0][c32], O[0][dt], 0, 0, 0);
;             O[1][dt] = __builtin_amdgcn_mfma_f32_16x16x32_bf16(vf, pf[1][c32], O[1][dt], 0, 0, 0); }
	v_mfma_f32_16x16x32_bf16 v[84:87], v[116:119], v[54:57], v[84:87]
	v_mfma_f32_16x16x32_bf16 v[84:87], v[120:123], v[58:61], v[84:87]
	v_mfma_f32_16x16x32_bf16 v[88:91], v[124:127], v[54:57], v[88:91]
	v_mfma_f32_16x16x32_bf16 v[88:91], v[128:131], v[58:61], v[88:91]
	v_lshlrev_b32_e32 v254, 6, v186
	v_sub_u32_e32 v254, v83, v254
	ds_read2_b32 v[200:201], v83 offset0:0 offset1:4
	ds_read2_b32 v[202:203], v83 offset0:8 offset1:12
	ds_read2_b32 v[204:205], v83 offset0:64 offset1:68
	ds_read2_b32 v[206:207], v83 offset0:72 offset1:76
	ds_read2_b32 v[62:63], v83 offset0:128 offset1:132
	ds_read2_b32 v[64:65], v83 offset0:136 offset1:140
	ds_read2_b32 v[66:67], v83 offset0:192 offset1:196
	ds_read2_b32 v[68:69], v83 offset0:200 offset1:204
	ds_read_b32 v199, v254 offset:1024
	s_waitcnt lgkmcnt(9)
	v_mfma_f32_16x16x32_bf16 v[92:95], v[132:135], v[54:57], v[92:95]
	v_mfma_f32_16x16x32_bf16 v[92:95], v[136:139], v[58:61], v[92:95]
	v_mfma_f32_16x16x32_bf16 v[96:99], v[140:143], v[54:57], v[96:99]
	v_mfma_f32_16x16x32_bf16 v[96:99], v[144:147], v[58:61], v[96:99]
	s_nop 1
	s_waitcnt lgkmcnt(0)
	v_add_f32_e32 v200, v200, v84
	v_add_f32_e32 v201, v201, v85
	v_add_f32_e32 v202, v202, v86
	v_add_f32_e32 v203, v203, v87
	v_add_f32_e32 v204, v204, v88
	v_add_f32_e32 v205, v205, v89
	v_add_f32_e32 v206, v206, v90
	v_add_f32_e32 v207, v207, v91
	v_add_f32_e32 v199, v199, v100
	v_add_f32_e32 v62, v62, v92
	v_add_f32_e32 v63, v63, v93
	v_add_f32_e32 v64, v64, v94
	v_add_f32_e32 v65, v65, v95
	v_add_f32_e32 v66, v66, v96
	v_add_f32_e32 v67, v67, v97
	v_add_f32_e32 v68, v68, v98
	v_add_f32_e32 v69, v69, v99
	v_cmp_ne_u32_e32 vcc, 0, v79
	s_and_saveexec_b64 s[84:85], vcc
	ds_write2_b32 v83, v200, v201 offset0:0 offset1:4
	ds_write2_b32 v83, v202, v203 offset0:8 offset1:12
	ds_write2_b32 v83, v204, v205 offset0:64 offset1:68
	ds_write2_b32 v83, v206, v207 offset0:72 offset1:76
	ds_write2_b32 v83, v62, v63 offset0:128 offset1:132
	ds_write2_b32 v83, v64, v65 offset0:136 offset1:140
	ds_write2_b32 v83, v66, v67 offset0:192 offset1:196
	ds_write2_b32 v83, v68, v69 offset0:200 offset1:204
	ds_write_b32 v254, v199 offset:1024
	s_mov_b64 exec, s[84:85]
	s_nop 3
	s_mov_b32 s100, -1
	s_add_i32 s21, s91, 8
	s_andn2_b64 s[84:85], s[12:13], s[14:15]
	s_bcnt1_i32_b64 s77, s[84:85]
	v_mbcnt_lo_u32_b32 v80, s84, 0
	v_mbcnt_hi_u32_b32 v80, s85, v80
	v_mov_b32_e32 v56, s77
	s_and_b64 s[84:85], s[12:13], s[14:15]
	s_bcnt1_i32_b64 s32, s[84:85]
	v_mbcnt_lo_u32_b32 v56, s84, v56
	v_mbcnt_hi_u32_b32 v56, s85, v56
	s_add_i32 s77, s77, s32
	v_cndmask_b32_e64 v80, v80, v56, s[84:85]
	v_mov_b32_e32 v56, s77
	s_andn2_b64 s[84:85], s[14:15], s[12:13]
	v_mbcnt_lo_u32_b32 v56, s84, v56
	v_mbcnt_hi_u32_b32 v56, s85, v56
	s_nop 0
	v_cndmask_b32_e64 v80, v80, v56, s[84:85]
	v_cndmask_b32_e64 v58, 0, 1, s[12:13]
	v_cndmask_b32_e64 v59, 0, 2, s[14:15]
	v_or_b32_e32 v58, v58, v59
	v_and_b32_e32 v59, 63, v185
	v_lshl_or_b32 v58, v58, 6, v59
	s_lshl_b32 s77, s91, 6
	s_add_i32 s77, s77, 0x20900
	v_add_u32_e32 v59, s77, v80
	s_and_saveexec_b64 s[84:85], s[22:23]
	ds_write_b8 v59, v58
	s_mov_b64 exec, s[84:85]
	s_lshl_b32 s32, s21, 2
	s_bcnt1_i32_b64 s84, s[22:23]
	v_lshrrev_b32_e32 v58, 2, v250
	v_add_u32_e32 v58, s32, v58
	v_cmp_gt_u32_e32 vcc, s84, v58
	v_add_u32_e32 v59, s77, v58
	ds_read_u8 v63, v59
	v_cndmask_b32_e64 v60, -1, 0, vcc
	s_waitcnt lgkmcnt(0)
	v_or_b32_e32 v63, v63, v60
	v_lshrrev_b32_e32 v56, 31, v63
	v_xor_b32_e32 v56, 1, v56
	v_max_i32_e32 v55, 0, v63
	v_mov_b32_e32 v79, v56
	v_and_b32_e32 v54, 63, v55
	v_bfe_u32 v58, v55, 6, 1
	v_bfe_u32 v59, v55, 7, 1
	v_lshlrev_b32_e32 v60, 11, v54
	v_mov_b32_e32 v61, 0
	v_lshl_add_u64 v[60:61], v[60:61], 0, v[246:247]
	global_load_dwordx4 v[104:107], v[60:61], off
	global_load_dwordx4 v[108:111], v[60:61], off offset:64
	v_lshl_add_u32 v63, v54, 4, v249
	ds_read_b32 v199, v63
	v_mul_u32_u24_e32 v83, 0x410, v54
	v_cmp_ne_u32_e32 vcc, 0, v58
	v_add_u32_e32 v83, v83, v248
	s_nop 0
	v_cndmask_b32_e32 v81, v2, v154, vcc
	s_cmp_lg_u64 vcc, 0
	s_cselect_b32 s21, 1, 0
	v_cmp_ne_u32_e32 vcc, 0, v59
	s_nop 1
	v_cndmask_b32_e32 v82, v2, v154, vcc
	s_cmp_lg_u64 vcc, 0
	s_cselect_b32 s32, 1, 0
	s_waitcnt vmcnt(0)
	s_and_b32 s83, s1, 0x4000
	v_add_u32_e32 v148, s83, v192
	v_add_u32_e32 v149, v148, v195
	v_add_u32_e32 v148, v148, v193
	ds_read_b128 v[116:119], v148
	ds_read_b128 v[120:123], v149
	ds_read_b128 v[124:127], v148 offset:2048
	ds_read_b128 v[128:131], v149 offset:2048
	ds_read_b128 v[132:135], v148 offset:4096
	ds_read_b128 v[136:139], v149 offset:4096
	ds_read_b128 v[140:143], v148 offset:6144
	ds_read_b128 v[144:147], v149 offset:6144
	v_add_u32_e32 v208, s99, v192
	v_add_u32_e32 v209, v208, v195
	v_add_u32_e32 v208, v208, v193
	ds_read_b128 v[38:41], v208
	ds_read_b128 v[42:45], v209
	ds_read_b128 v[46:49], v208 offset:2048
	ds_read_b128 v[50:53], v209 offset:2048
	s_waitcnt lgkmcnt(12)
	v_sub_f32_e32 v81, v81, v199
	v_sub_f32_e32 v82, v82, v199
	v_mov_b32_e32 v70, v81
	v_mov_b32_e32 v71, v81
	v_mov_b32_e32 v72, v81
	v_mov_b32_e32 v73, v81
	v_mov_b32_e32 v74, v81
	v_mov_b32_e32 v75, v81
	v_mov_b32_e32 v76, v81
	v_mov_b32_e32 v77, v81
	v_mov_b32_e32 v200, v81
	v_mov_b32_e32 v201, v81
	v_mov_b32_e32 v202, v81
	v_mov_b32_e32 v203, v81
	v_mov_b32_e32 v204, v81
	v_mov_b32_e32 v205, v81
	v_mov_b32_e32 v206, v81
	v_mov_b32_e32 v207, v81
	v_mov_b32_e32 v54, v82
	v_mov_b32_e32 v55, v82
	v_mov_b32_e32 v56, v82
	v_mov_b32_e32 v57, v82
	v_mov_b32_e32 v58, v82
	v_mov_b32_e32 v59, v82
	v_mov_b32_e32 v60, v82
	v_mov_b32_e32 v61, v82
	v_mov_b32_e32 v62, v82
	v_mov_b32_e32 v63, v82
	v_mov_b32_e32 v64, v82
	v_mov_b32_e32 v65, v82
	v_mov_b32_e32 v66, v82
	v_mov_b32_e32 v67, v82
	v_mov_b32_e32 v68, v82
	v_mov_b32_e32 v69, v82
	s_waitcnt lgkmcnt(10)
; __device__ __forceinline__ float ex2(float x) { return __builtin_amdgcn_exp2f(x); }
; template <bool SELMASK>
; __device__ __forceinline__ void attn_far_fast(const LAS unsigned char* kb, const LAS unsigned char* vb, const bf16x8 (&qf)[2][2], int col, int q, float bias_far, bool sel0, bool sel1, Softmax (&st)[2], f32x4 (&O)[2][4]) {
;     ...
; #pragma unroll
;     for (int kt = 0; kt < 4; ++kt) { const bf16x8 k0 = lds_frag(kb, 16 * kt + col, q), k1 = lds_frag(kb, 16 * kt + col, 4 + q);
; #pragma unroll
;         for (int c = 0; c < 2; ++c) { S[c][kt] = __builtin_amdgcn_mfma_f32_16x16x32_bf16(k0, qf[c][0], z4, 0, 0, 0); S[c][kt] = __builtin_amdgcn_mfma_f32_16x16x32_bf16(k1, qf[c][1], S[c][kt], 0, 0, 0); } }
;     bf16x8 pf[2][2];
; #pragma unroll
;     for (int c = 0; c < 2; ++c) {
;         const bool sel = c == 0 ? sel0 : sel1;
;         const float off = ((SELMASK && !sel) ? NEG : bias_far) - st[c].m;
; #pragma unroll
;         for (int kt = 0; kt < 4; ++kt) { f32x4 p = S[c][kt] + off;
; #pragma unroll
;             for (int e = 0; e < 4; ++e) p[e] = ex2(p[e]);
;             S[c][kt] = p; }
;         pf[c][0] = pack8(S[c][0], S[c][1]); pf[c][1] = pack8(S[c][2], S[c][3]);
;         st[c].l = __builtin_amdgcn_mfma_f32_16x16x32_bf16(ONES8, pf[c][0], st[c].l, 0, 0, 0); st[c].l = __builtin_amdgcn_mfma_f32_16x16x32_bf16(ONES8, pf[c][1], st[c].l, 0, 0, 0);
;     }
; #pragma unroll
;     for (int c32 = 0; c32 < 2; ++c32)
; #pragma unroll
;         for (int dt = 0; dt < 4; ++dt) { const bf16x8 vf = lds_frag(vb, 16 * dt + col, 4 * c32 + q);
;             O[0][dt] = __builtin_amdgcn_mfma_f32_16x16x32_bf16(vf, pf[0][c32], O[0][dt], 0, 0, 0);
;             O[1][dt] = __builtin_amdgcn_mfma_f32_16x16x32_bf16(vf, pf[1][c32], O[1][dt], 0, 0, 0); }
	v_mfma_f32_16x16x32_bf16 v[70:73], v[116:119], v[104:107], v[70:73]
	v_mfma_f32_16x16x32_bf16 v[70:73], v[120:123], v[108:111], v[70:73]
	s_waitcnt lgkmcnt(8)
	v_mfma_f32_16x16x32_bf16 v[74:77], v[124:127], v[104:107], v[74:77]
	v_mfma_f32_16x16x32_bf16 v[74:77], v[128:131], v[108:111], v[74:77]
	ds_read_b128 v[116:119], v148 offset:32768
	ds_read_b128 v[120:123], v149 offset:32768
	ds_read_b128 v[124:127], v148 offset:34816
	ds_read_b128 v[128:131], v149 offset:34816
	s_waitcnt lgkmcnt(10)
	v_mfma_f32_16x16x32_bf16 v[200:203], v[132:135], v[104:107], v[200:203]
	v_mfma_f32_16x16x32_bf16 v[200:203], v[136:139], v[108:111], v[200:203]
	s_waitcnt lgkmcnt(8)
	v_mfma_f32_16x16x32_bf16 v[204:207], v[140:143], v[104:107], v[204:207]
	v_mfma_f32_16x16x32_bf16 v[204:207], v[144:147], v[108:111], v[204:207]
	ds_read_b128 v[132:135], v148 offset:36864
	ds_read_b128 v[136:139], v149 offset:36864
	ds_read_b128 v[140:143], v148 offset:38912
	ds_read_b128 v[144:147], v149 offset:38912
	s_waitcnt lgkmcnt(10)
	v_mfma_f32_16x16x32_bf16 v[54:57], v[38:41], v[104:107], v[54:57]
	v_mfma_f32_16x16x32_bf16 v[54:57], v[42:45], v[108:111], v[54:57]
	s_waitcnt lgkmcnt(8)
	v_mfma_f32_16x16x32_bf16 v[58:61], v[46:49], v[104:107], v[58:61]
	v_mfma_f32_16x16x32_bf16 v[58:61], v[50:53], v[108:111], v[58:61]
	ds_read_b128 v[38:41], v208 offset:4096
	ds_read_b128 v[42:45], v209 offset:4096
	ds_read_b128 v[46:49], v208 offset:6144
	ds_read_b128 v[50:53], v209 offset:6144
	v_exp_f32_e32 v70, v70
	v_exp_f32_e32 v71, v71
	v_exp_f32_e32 v72, v72
	v_exp_f32_e32 v73, v73
	v_exp_f32_e32 v74, v74
	v_exp_f32_e32 v75, v75
	v_exp_f32_e32 v76, v76
	v_exp_f32_e32 v77, v77
	v_exp_f32_e32 v200, v200
	v_exp_f32_e32 v201, v201
	v_exp_f32_e32 v202, v202
	v_exp_f32_e32 v203, v203
	v_exp_f32_e32 v204, v204
	v_exp_f32_e32 v205, v205
	v_exp_f32_e32 v206, v206
	v_exp_f32_e32 v207, v207
	s_nop 0
	v_cvt_pk_bf16_f32 v70, v70, v71
	v_cvt_pk_bf16_f32 v71, v72, v73
	v_cvt_pk_bf16_f32 v72, v74, v75
	v_cvt_pk_bf16_f32 v73, v76, v77
	v_cvt_pk_bf16_f32 v74, v200, v201
	v_cvt_pk_bf16_f32 v75, v202, v203
	v_cvt_pk_bf16_f32 v76, v204, v205
	v_cvt_pk_bf16_f32 v77, v206, v207
	s_nop 1
	v_mfma_f32_16x16x32_bf16 v[100:103], v[112:115], v[70:73], 0
	v_mfma_f32_16x16x32_bf16 v[100:103], v[112:115], v[74:77], v[100:103]
	s_waitcnt lgkmcnt(4)
	v_mfma_f32_16x16x32_bf16 v[84:87], v[116:119], v[70:73], 0
	v_mfma_f32_16x16x32_bf16 v[84:87], v[120:123], v[74:77], v[84:87]
	v_mfma_f32_16x16x32_bf16 v[88:91], v[124:127], v[70:73], 0
	v_mfma_f32_16x16x32_bf16 v[88:91], v[128:131], v[74:77], v[88:91]
	v_mfma_f32_16x16x32_bf16 v[92:95], v[132:135], v[70:73], 0
	v_mfma_f32_16x16x32_bf16 v[92:95], v[136:139], v[74:77], v[92:95]
	v_mfma_f32_16x16x32_bf16 v[96:99], v[140:143], v[70:73], 0
	v_mfma_f32_16x16x32_bf16 v[96:99], v[144:147], v[74:77], v[96:99]
	s_waitcnt lgkmcnt(2)
	v_mfma_f32_16x16x32_bf16 v[62:65], v[38:41], v[104:107], v[62:65]
	v_mfma_f32_16x16x32_bf16 v[62:65], v[42:45], v[108:111], v[62:65]
	s_waitcnt lgkmcnt(0)
	v_mfma_f32_16x16x32_bf16 v[66:69], v[46:49], v[104:107], v[66:69]
	v_mfma_f32_16x16x32_bf16 v[66:69], v[50:53], v[108:111], v[66:69]
	ds_read_b128 v[116:119], v208 offset:32768
	ds_read_b128 v[120:123], v209 offset:32768
	ds_read_b128 v[124:127], v208 offset:34816
	ds_read_b128 v[128:131], v209 offset:34816
	ds_read_b128 v[132:135], v208 offset:36864
	ds_read_b128 v[136:139], v209 offset:36864
	ds_read_b128 v[140:143], v208 offset:38912
	ds_read_b128 v[144:147], v209 offset:38912
	s_nop 3
	v_exp_f32_e32 v54, v54
	v_exp_f32_e32 v55, v55
	v_exp_f32_e32 v56, v56
	v_exp_f32_e32 v57, v57
	v_exp_f32_e32 v58, v58
	v_exp_f32_e32 v59, v59
	v_exp_f32_e32 v60, v60
	v_exp_f32_e32 v61, v61
	v_exp_f32_e32 v62, v62
	v_exp_f32_e32 v63, v63
	v_exp_f32_e32 v64, v64
	v_exp_f32_e32 v65, v65
	v_exp_f32_e32 v66, v66
	v_exp_f32_e32 v67, v67
	v_exp_f32_e32 v68, v68
	v_exp_f32_e32 v69, v69
	s_nop 0
	v_cvt_pk_bf16_f32 v54, v54, v55
	v_cvt_pk_bf16_f32 v55, v56, v57
	v_cvt_pk_bf16_f32 v56, v58, v59
	v_cvt_pk_bf16_f32 v57, v60, v61
	v_cvt_pk_bf16_f32 v58, v62, v63
	v_cvt_pk_bf16_f32 v59, v64, v65
	v_cvt_pk_bf16_f32 v60, v66, v67
	v_cvt_pk_bf16_f32 v61, v68, v69
	s_nop 1
	v_mfma_f32_16x16x32_bf16 v[100:103], v[112:115], v[54:57], v[100:103]
	v_mfma_f32_16x16x32_bf16 v[100:103], v[112:115], v[58:61], v[100:103]
	s_waitcnt lgkmcnt(4)
	v_mfma_f32_16x16x32_bf16 v[84:87], v[116:119], v[54:57], v[84:87]
	v_mfma_f32_16x16x32_bf16 v[84:87], v[120:123], v[58:61], v[84:87]
	v_mfma_f32_16x16x32_bf16 v[88:91], v[124:127], v[54:57], v[88:91]
	v_mfma_f32_16x16x32_bf16 v[88:91], v[128:131], v[58:61], v[88:91]
	v_lshlrev_b32_e32 v254, 6, v186
	v_sub_u32_e32 v254, v83, v254
	ds_read2_b32 v[200:201], v83 offset0:0 offset1:4
	ds_read2_b32 v[202:203], v83 offset0:8 offset1:12
	ds_read2_b32 v[204:205], v83 offset0:64 offset1:68
	ds_read2_b32 v[206:207], v83 offset0:72 offset1:76
	ds_read2_b32 v[62:63], v83 offset0:128 offset1:132
	ds_read2_b32 v[64:65], v83 offset0:136 offset1:140
	ds_read2_b32 v[66:67], v83 offset0:192 offset1:196
	ds_read2_b32 v[68:69], v83 offset0:200 offset1:204
	ds_read_b32 v199, v254 offset:1024
	s_waitcnt lgkmcnt(9)
	v_mfma_f32_16x16x32_bf16 v[92:95], v[132:135], v[54:57], v[92:95]
	v_mfma_f32_16x16x32_bf16 v[92:95], v[136:139], v[58:61], v[92:95]
	v_mfma_f32_16x16x32_bf16 v[96:99], v[140:143], v[54:57], v[96:99]
	v_mfma_f32_16x16x32_bf16 v[96:99], v[144:147], v[58:61], v[96:99]
	s_nop 1
	s_waitcnt lgkmcnt(0)
	v_add_f32_e32 v200, v200, v84
	v_add_f32_e32 v201, v201, v85
	v_add_f32_e32 v202, v202, v86
	v_add_f32_e32 v203, v203, v87
	v_add_f32_e32 v204, v204, v88
	v_add_f32_e32 v205, v205, v89
	v_add_f32_e32 v206, v206, v90
	v_add_f32_e32 v207, v207, v91
	v_add_f32_e32 v199, v199, v100
	v_add_f32_e32 v62, v62, v92
	v_add_f32_e32 v63, v63, v93
	v_add_f32_e32 v64, v64, v94
	v_add_f32_e32 v65, v65, v95
	v_add_f32_e32 v66, v66, v96
	v_add_f32_e32 v67, v67, v97
	v_add_f32_e32 v68, v68, v98
	v_add_f32_e32 v69, v69, v99
	v_cmp_ne_u32_e32 vcc, 0, v79
	s_and_saveexec_b64 s[84:85], vcc
	ds_write2_b32 v83, v200, v201 offset0:0 offset1:4
	ds_write2_b32 v83, v202, v203 offset0:8 offset1:12
	ds_write2_b32 v83, v204, v205 offset0:64 offset1:68
	ds_write2_b32 v83, v206, v207 offset0:72 offset1:76
	ds_write2_b32 v83, v62, v63 offset0:128 offset1:132
	ds_write2_b32 v83, v64, v65 offset0:136 offset1:140
	ds_write2_b32 v83, v66, v67 offset0:192 offset1:196
	ds_write2_b32 v83, v68, v69 offset0:200 offset1:204
	ds_write_b32 v254, v199 offset:1024
	s_mov_b64 exec, s[84:85]
	s_nop 3

.Lbm_noitem:
	s_mov_b32 s83, -1
	s_add_i32 s77, s75, 2
	s_cmp_gt_i32 s77, s26
	s_cbranch_scc1 .Lbm_g1_end_nb
	s_lshr_b32 s21, s77, 5
	v_mov_b32_e32 v255, v242
	s_cmp_eq_u32 s21, 1
	s_cselect_b64 vcc, -1, 0
	v_cndmask_b32_e32 v255, v255, v243, vcc
	s_cmp_eq_u32 s21, 2
	s_cselect_b64 vcc, -1, 0
	v_cndmask_b32_e32 v255, v255, v244, vcc
	s_cmp_eq_u32 s21, 3
	s_cselect_b64 vcc, -1, 0
	v_cndmask_b32_e32 v255, v255, v245, vcc
	s_and_b32 s21, s77, 31
	s_lshl_b32 s21, 1, s21
	s_lshl_b32 s32, s21, 1
	v_and_b32_e32 v80, s21, v255
	v_cmp_ne_u32_e64 s[12:13], 0, v80
	v_and_b32_e32 v80, s32, v255
	v_cmp_ne_u32_e64 s[14:15], 0, v80
	s_nop 3
	s_or_b64 s[22:23], s[12:13], s[14:15]
	s_bcnt1_i32_b64 s11, s[22:23]
	s_add_i32 s11, s11, 3
	s_lshr_b32 s11, s11, 2
	s_cmp_ge_u32 s91, s11
	s_cbranch_scc1 .Lbm_g1_end_nb
	s_add_i32 s83, s91, 8
	s_cmp_lt_u32 s83, s11
	s_cselect_b32 s83, 0x10000, 0
	s_add_i32 s83, s83, s75
	s_add_i32 s83, s83, 2
	s_andn2_b64 s[84:85], s[12:13], s[14:15]
	s_bcnt1_i32_b64 s77, s[84:85]
	v_mbcnt_lo_u32_b32 v80, s84, 0
	v_mbcnt_hi_u32_b32 v80, s85, v80
	v_mov_b32_e32 v255, s77
	s_and_b64 s[84:85], s[12:13], s[14:15]
	s_bcnt1_i32_b64 s32, s[84:85]
	v_mbcnt_lo_u32_b32 v255, s84, v255
	v_mbcnt_hi_u32_b32 v255, s85, v255
	s_add_i32 s77, s77, s32
	v_cndmask_b32_e64 v80, v80, v255, s[84:85]
	v_mov_b32_e32 v255, s77
	s_andn2_b64 s[84:85], s[14:15], s[12:13]
	v_mbcnt_lo_u32_b32 v255, s84, v255
	v_mbcnt_hi_u32_b32 v255, s85, v255
	s_nop 0
	v_cndmask_b32_e64 v80, v80, v255, s[84:85]
	v_cndmask_b32_e64 v78, 0, 1, s[12:13]
	v_cndmask_b32_e64 v255, 0, 2, s[14:15]
	v_or_b32_e32 v78, v78, v255
	v_and_b32_e32 v255, 63, v185
	v_lshl_or_b32 v78, v78, 6, v255
	s_lshl_b32 s77, s91, 6
	s_add_i32 s77, s77, 0x20900
	v_add_u32_e32 v255, s77, v80
	s_and_saveexec_b64 s[84:85], s[22:23]
	ds_write_b8 v255, v78
	s_mov_b64 exec, s[84:85]
	s_lshl_b32 s32, s91, 2
	s_bcnt1_i32_b64 s84, s[22:23]
	v_lshrrev_b32_e32 v78, 2, v250
	v_add_u32_e32 v78, s32, v78
	v_cmp_gt_u32_e32 vcc, s84, v78
	v_add_u32_e32 v255, s77, v78
	ds_read_u8 v251, v255
	v_cndmask_b32_e64 v254, -1, 0, vcc
.Lbm_g1_end_nb:
	s_mov_b32 s100, -1
	s_cmp_lt_i32 s83, 0
	s_cbranch_scc1 .Lbm_g2_end_nb
	s_waitcnt lgkmcnt(0)
	v_or_b32_e32 v251, v251, v254
	v_max_i32_e32 v254, 0, v251
	v_and_b32_e32 v254, 63, v254
	v_lshlrev_b32_e32 v254, 11, v254
	v_mov_b32_e32 v255, 0
	v_lshl_add_u64 v[254:255], v[254:255], 0, v[246:247]
	global_load_dwordx4 v[104:107], v[254:255], off
	global_load_dwordx4 v[108:111], v[254:255], off offset:64
	s_mov_b32 s100, s83
